# v55 + router top-k merge shuffles via DPP + P2b: cnt[e] taken from the LDS row-base table instead of a global load, chunk-top waits count the Y stores actually issued
# baseline (speedup 1.0000x reference)
.LBB0_354:
	s_ashr_i32 s11, s10, 31
	s_lshl_b32 s12, s10, 2
	s_add_i32 s12, s12, 0
	s_add_i32 s13, s12, 0x21400
	v_mov_b32_e32 v35, s13
	ds_read_b32 v35, v35
	s_waitcnt lgkmcnt(0)
	v_readfirstlane_b32 s17, v35
	s_sub_i32 s14, s14, s17
	s_add_i32 s13, s12, 0x21000
	v_mov_b32_e32 v34, s13
	ds_read2_b32 v[34:35], v34 offset1:1
	s_waitcnt lgkmcnt(0)
	v_readfirstlane_b32 s13, v35
	v_readfirstlane_b32 s99, v34
	s_sub_i32 s13, s13, s99
	s_sub_i32 s99, 0x20000, s99
	s_cmp_eq_u32 s10, 0xff
	s_cselect_b32 s13, s99, s13
	s_add_i32 s15, s13, 0x17f
	s_mul_hi_i32 s15, s15, 0x2aaaaaab
	s_lshr_b32 s16, s15, 31
	s_ashr_i32 s15, s15, 6
	s_add_i32 s15, s15, s16
	s_abs_i32 s16, s15
	v_cvt_f32_u32_e32 v34, s16
	s_sub_i32 s18, 0, s16
	s_add_i32 s17, s13, s15
	s_add_i32 s17, s17, -1
	v_rcp_iflag_f32_e32 v34, v34
	s_xor_b32 s15, s17, s15
	s_abs_i32 s17, s17
	s_ashr_i32 s15, s15, 31
	v_mul_f32_e32 v34, 0x4f7ffffe, v34
	v_cvt_u32_f32_e32 v34, v34
	s_nop 0
	v_readfirstlane_b32 s19, v34
	s_mul_i32 s18, s18, s19
	s_mul_hi_u32 s18, s19, s18
	s_add_i32 s19, s19, s18
	s_mul_hi_u32 s18, s17, s19
	s_mul_i32 s19, s18, s16
	s_sub_i32 s17, s17, s19
	s_add_i32 s20, s18, 1
	s_sub_i32 s19, s17, s16
	s_cmp_ge_u32 s17, s16
	s_cselect_b32 s18, s20, s18
	s_cselect_b32 s17, s19, s17
	s_add_i32 s19, s18, 1
	s_cmp_ge_u32 s17, s16
	s_cselect_b32 s16, s19, s18
	s_xor_b32 s16, s16, s15
	s_sub_i32 s15, s16, s15
	s_add_i32 s15, s15, 15
	s_and_b32 s15, s15, -16
	s_mul_i32 s38, s15, s14
	s_sub_i32 s13, s13, s38
	s_min_i32 s36, s13, s15
	s_cmp_lt_i32 s36, 1
	s_cbranch_scc1 .LBB0_378
	s_add_i32 s12, s12, 0x21000
	v_mov_b32_e32 v34, s12
	s_add_i32 s13, s36, 15
	ds_read_b32 v193, v34
	s_lshr_b32 s37, s13, 4
	s_add_i32 s13, s37, 7
	s_lshr_b32 s13, s13, 3
	s_lshl_b64 s[34:35], s[10:11], 20
	s_lshl_b64 s[40:41], s[10:11], 16
	s_ashr_i32 s39, s38, 31
	s_cmp_lt_i32 s13, 2
	s_mov_b64 s[10:11], -1
	s_cbranch_scc1 .LBB0_400
	s_cmp_lg_u32 s13, 2
	s_cbranch_scc0 .LBB0_380
	v_mov_b32_e32 v165, v0
	s_waitcnt lgkmcnt(0)
	v_add_u32_e32 v38, s38, v193
	v_readfirstlane_b32 s10, v165
	s_ashr_i32 s12, s10, 6
	v_and_b32_e32 v167, 15, v165
	s_mul_i32 s20, s12, 48
	v_or_b32_e32 v36, s20, v167
	v_cmp_gt_i32_e32 vcc, s36, v36
	v_and_b32_e32 v162, 48, v165
	v_lshl_add_u64 v[34:35], s[24:25], 0, v[162:163]
	v_cndmask_b32_e32 v36, 0, v36, vcc
	v_add_u32_e32 v36, v36, v38
	v_ashrrev_i32_e32 v37, 31, v36
	v_lshlrev_b64 v[36:37], 9, v[36:37]
	v_lshl_add_u64 v[36:37], v[34:35], 0, v[36:37]
	s_add_i32 s10, s20, 16
	global_load_dwordx4 v[66:69], v[36:37], off
	global_load_dwordx4 v[70:73], v[36:37], off offset:64
	global_load_dwordx4 v[74:77], v[36:37], off offset:128
	global_load_dwordx4 v[78:81], v[36:37], off offset:192
	global_load_dwordx4 v[82:85], v[36:37], off offset:256
	global_load_dwordx4 v[86:89], v[36:37], off offset:320
	global_load_dwordx4 v[90:93], v[36:37], off offset:384
	global_load_dwordx4 v[94:97], v[36:37], off offset:448
	v_or_b32_e32 v36, s10, v167
	v_cmp_gt_i32_e32 vcc, s36, v36
	s_add_i32 s10, s20, 32
	v_bfe_u32 v176, v165, 3, 3
	v_cndmask_b32_e32 v36, 0, v36, vcc
	v_add_u32_e32 v36, v36, v38
	v_ashrrev_i32_e32 v37, 31, v36
	v_lshlrev_b64 v[36:37], 9, v[36:37]
	v_lshl_add_u64 v[36:37], v[34:35], 0, v[36:37]
	global_load_dwordx4 v[98:101], v[36:37], off
	global_load_dwordx4 v[102:105], v[36:37], off offset:64
	global_load_dwordx4 v[106:109], v[36:37], off offset:128
	global_load_dwordx4 v[110:113], v[36:37], off offset:192
	global_load_dwordx4 v[114:117], v[36:37], off offset:256
	global_load_dwordx4 v[118:121], v[36:37], off offset:320
	global_load_dwordx4 v[122:125], v[36:37], off offset:384
	global_load_dwordx4 v[126:129], v[36:37], off offset:448
	v_or_b32_e32 v36, s10, v167
	v_cmp_gt_i32_e32 vcc, s36, v36
	v_or_b32_e32 v44, s20, v176
	s_add_u32 s13, s6, s40
	v_cndmask_b32_e32 v36, 0, v36, vcc
	v_add_u32_e32 v36, v36, v38
	v_ashrrev_i32_e32 v37, 31, v36
	v_lshlrev_b64 v[36:37], 9, v[36:37]
	v_lshl_add_u64 v[34:35], v[34:35], 0, v[36:37]
	v_or_b32_e32 v36, 8, v44
	s_addc_u32 s15, s7, s41
	s_lshl_b64 s[10:11], s[38:39], 2
	v_cmp_gt_i32_e32 vcc, s36, v36
	v_add_u32_e32 v38, 16, v44
	s_add_u32 s14, s13, s10
	v_cndmask_b32_e32 v36, 0, v36, vcc
	v_cmp_gt_i32_e32 vcc, s36, v38
	v_add_u32_e32 v40, 24, v44
	s_addc_u32 s15, s15, s11
	v_cmp_gt_i32_e64 s[10:11], s36, v44
	v_cndmask_b32_e32 v38, 0, v38, vcc
	v_cmp_gt_i32_e32 vcc, s36, v40
	v_add_u32_e32 v42, 32, v44
	global_load_dwordx4 v[130:133], v[34:35], off
	global_load_dwordx4 v[134:137], v[34:35], off offset:64
	global_load_dwordx4 v[138:141], v[34:35], off offset:128
	global_load_dwordx4 v[142:145], v[34:35], off offset:192
	global_load_dwordx4 v[146:149], v[34:35], off offset:256
	global_load_dwordx4 v[150:153], v[34:35], off offset:320
	global_load_dwordx4 v[154:157], v[34:35], off offset:384
	global_load_dwordx4 v[158:161], v[34:35], off offset:448
	v_cndmask_b32_e64 v34, 0, v44, s[10:11]
	v_cndmask_b32_e32 v40, 0, v40, vcc
	v_cmp_gt_i32_e32 vcc, s36, v42
	v_add_u32_e32 v44, 40, v44
	v_ashrrev_i32_e32 v35, 31, v34
	v_cndmask_b32_e32 v42, 0, v42, vcc
	v_cmp_gt_i32_e32 vcc, s36, v44
	v_lshl_add_u64 v[34:35], v[34:35], 2, s[14:15]
	v_ashrrev_i32_e32 v37, 31, v36
	v_cndmask_b32_e32 v44, 0, v44, vcc
	v_ashrrev_i32_e32 v39, 31, v38
	v_ashrrev_i32_e32 v41, 31, v40
	v_ashrrev_i32_e32 v43, 31, v42
	v_ashrrev_i32_e32 v45, 31, v44
	v_lshl_add_u64 v[36:37], v[36:37], 2, s[14:15]
	v_lshl_add_u64 v[38:39], v[38:39], 2, s[14:15]
	v_lshl_add_u64 v[40:41], v[40:41], 2, s[14:15]
	v_lshl_add_u64 v[42:43], v[42:43], 2, s[14:15]
	v_lshl_add_u64 v[44:45], v[44:45], 2, s[14:15]
	global_load_dword v174, v[34:35], off
	global_load_dword v172, v[36:37], off
	global_load_dword v170, v[38:39], off
	global_load_dword v168, v[40:41], off
	global_load_dword v166, v[42:43], off
	global_load_dword v164, v[44:45], off
	v_ashrrev_i32_e32 v34, 4, v165
	v_lshrrev_b32_e32 v36, 2, v34
	v_bfe_u32 v169, v165, 2, 2
	v_bfe_u32 v35, v34, 1, 1
	v_and_b32_e32 v36, 2, v36
	v_bitop3_b32 v35, v35, v169, v36 bitop3:0x36
	v_lshlrev_b32_e32 v36, 3, v165
	v_lshlrev_b32_e32 v35, 5, v35
	v_and_b32_e32 v162, 24, v36
	s_add_u32 s42, s4, s34
	v_lshlrev_b32_e32 v36, 4, v167
	v_lshl_add_u32 v37, v34, 7, 0
	s_addc_u32 s43, s5, s35
	v_add3_u32 v194, v37, v35, v162
	v_lshl_or_b32 v195, v34, 12, v36
	s_andn2_b64 vcc, exec, s[30:31]
	v_mov_b32_e32 v34, v2
	v_mov_b32_e32 v35, v3
	v_mov_b32_e32 v36, v4
	v_mov_b32_e32 v37, v5
	v_mov_b32_e32 v38, v6
	v_mov_b32_e32 v39, v7
	v_mov_b32_e32 v40, v8
	v_mov_b32_e32 v41, v9
	v_mov_b32_e32 v42, v10
	v_mov_b32_e32 v43, v11
	v_mov_b32_e32 v44, v12
	v_mov_b32_e32 v45, v13
	v_mov_b32_e32 v46, v14
	v_mov_b32_e32 v47, v15
	v_mov_b32_e32 v48, v16
	v_mov_b32_e32 v49, v17
	v_mov_b32_e32 v50, v18
	v_mov_b32_e32 v51, v19
	v_mov_b32_e32 v52, v20
	v_mov_b32_e32 v53, v21
	v_mov_b32_e32 v54, v22
	v_mov_b32_e32 v55, v23
	v_mov_b32_e32 v56, v24
	v_mov_b32_e32 v57, v25
	v_mov_b32_e32 v58, v26
	v_mov_b32_e32 v59, v27
	v_mov_b32_e32 v60, v28
	v_mov_b32_e32 v61, v29
	v_mov_b32_e32 v62, v30
	v_mov_b32_e32 v63, v31
	v_mov_b32_e32 v64, v32
	v_mov_b32_e32 v65, v33
	s_cbranch_vccnz .LBB0_359
	s_add_u32 s14, s42, 0x20000
	global_load_dwordx4 v[34:37], v195, s[42:43]
	s_addc_u32 s15, s43, 0
	global_load_dwordx4 v[38:41], v195, s[14:15]
	s_add_u32 s14, s42, 0x40000
	s_addc_u32 s15, s43, 0
	global_load_dwordx4 v[42:45], v195, s[14:15]
	s_add_u32 s14, s42, 0x60000
	s_addc_u32 s15, s43, 0
	global_load_dwordx4 v[46:49], v195, s[14:15]
	s_add_u32 s14, s42, 0x80000
	s_addc_u32 s15, s43, 0
	global_load_dwordx4 v[50:53], v195, s[14:15]
	s_add_u32 s14, s42, 0xa0000
	s_addc_u32 s15, s43, 0
	global_load_dwordx4 v[54:57], v195, s[14:15]
	s_add_u32 s14, s42, 0xc0000
	s_addc_u32 s15, s43, 0
	global_load_dwordx4 v[58:61], v195, s[14:15]
	s_add_u32 s14, s42, 0xe0000
	s_addc_u32 s15, s43, 0
	global_load_dwordx4 v[62:65], v195, s[14:15]
	s_add_u32 s14, s42, 0x100
	s_waitcnt vmcnt(0)
	s_addc_u32 s15, s43, 0
	v_cvt_pk_bf16_f32 v34, v34, v35
	v_cvt_pk_bf16_f32 v35, v36, v37
	v_cvt_pk_bf16_f32 v36, v38, v39
	v_cvt_pk_bf16_f32 v37, v40, v41
	ds_write2st64_b64 v194, v[34:35], v[36:37] offset1:8
	v_cvt_pk_bf16_f32 v34, v42, v43
	v_cvt_pk_bf16_f32 v35, v44, v45
	v_cvt_pk_bf16_f32 v36, v46, v47
	v_cvt_pk_bf16_f32 v37, v48, v49
	ds_write2st64_b64 v194, v[34:35], v[36:37] offset0:16 offset1:24
	v_cvt_pk_bf16_f32 v34, v50, v51
	v_cvt_pk_bf16_f32 v35, v52, v53
	v_cvt_pk_bf16_f32 v36, v54, v55
	v_cvt_pk_bf16_f32 v37, v56, v57
	ds_write2st64_b64 v194, v[34:35], v[36:37] offset0:32 offset1:40
	v_cvt_pk_bf16_f32 v34, v58, v59
	v_cvt_pk_bf16_f32 v35, v60, v61
	v_cvt_pk_bf16_f32 v36, v62, v63
	v_cvt_pk_bf16_f32 v37, v64, v65
	ds_write2st64_b64 v194, v[34:35], v[36:37] offset0:48 offset1:56
	global_load_dwordx4 v[34:37], v195, s[14:15]
	s_add_u32 s14, s42, 0x20100
	s_addc_u32 s15, s43, 0
	global_load_dwordx4 v[38:41], v195, s[14:15]
	s_add_u32 s14, s42, 0x40100
	s_addc_u32 s15, s43, 0
	global_load_dwordx4 v[42:45], v195, s[14:15]
	s_add_u32 s14, s42, 0x60100
	s_addc_u32 s15, s43, 0
	global_load_dwordx4 v[46:49], v195, s[14:15]
	s_add_u32 s14, s42, 0x80100
	s_addc_u32 s15, s43, 0
	global_load_dwordx4 v[50:53], v195, s[14:15]
	s_add_u32 s14, s42, 0xa0100
	s_addc_u32 s15, s43, 0
	global_load_dwordx4 v[54:57], v195, s[14:15]
	s_add_u32 s14, s42, 0xc0100
	s_addc_u32 s15, s43, 0
	global_load_dwordx4 v[58:61], v195, s[14:15]
	s_add_u32 s14, s42, 0xe0100
	s_addc_u32 s15, s43, 0
	global_load_dwordx4 v[62:65], v195, s[14:15]

.LBB0_960:
	s_ashr_i32 s11, s10, 31
	s_lshl_b32 s12, s10, 2
	s_add_i32 s12, s12, 0
	s_add_i32 s13, s12, 0x21400
	v_mov_b32_e32 v35, s13
	ds_read_b32 v35, v35
	s_waitcnt lgkmcnt(0)
	v_readfirstlane_b32 s16, v35
	s_sub_i32 s16, s79, s16
	s_add_i32 s13, s12, 0x21000
	v_mov_b32_e32 v34, s13
	ds_read2_b32 v[34:35], v34 offset1:1
	s_waitcnt lgkmcnt(0)
	v_readfirstlane_b32 s13, v35
	v_readfirstlane_b32 s99, v34
	s_sub_i32 s13, s13, s99
	s_sub_i32 s99, 0x20000, s99
	s_cmp_eq_u32 s10, 0xff
	s_cselect_b32 s13, s99, s13
	s_add_i32 s14, s13, 0x17f
	s_mul_hi_i32 s14, s14, 0x2aaaaaab
	s_lshr_b32 s15, s14, 31
	s_ashr_i32 s14, s14, 6
	s_add_i32 s14, s14, s15
	s_abs_i32 s15, s14
	v_cvt_f32_u32_e32 v34, s15
	s_sub_i32 s18, 0, s15
	s_add_i32 s17, s13, s14
	s_add_i32 s17, s17, -1
	v_rcp_iflag_f32_e32 v34, v34
	s_xor_b32 s14, s17, s14
	s_abs_i32 s17, s17
	s_ashr_i32 s14, s14, 31
	v_mul_f32_e32 v34, 0x4f7ffffe, v34
	v_cvt_u32_f32_e32 v34, v34
	s_nop 0
	v_readfirstlane_b32 s19, v34
	s_mul_i32 s18, s18, s19
	s_mul_hi_u32 s18, s19, s18
	s_add_i32 s19, s19, s18
	s_mul_hi_u32 s18, s17, s19
	s_mul_i32 s19, s18, s15
	s_sub_i32 s17, s17, s19
	s_add_i32 s20, s18, 1
	s_sub_i32 s19, s17, s15
	s_cmp_ge_u32 s17, s15
	s_cselect_b32 s18, s20, s18
	s_cselect_b32 s17, s19, s17
	s_add_i32 s19, s18, 1
	s_cmp_ge_u32 s17, s15
	s_cselect_b32 s15, s19, s18
	s_xor_b32 s15, s15, s14
	s_sub_i32 s14, s15, s14
	s_add_i32 s14, s14, 15
	s_and_b32 s14, s14, -16
	s_mul_i32 s34, s14, s16
	s_sub_i32 s13, s13, s34
	s_min_i32 s48, s13, s14
	s_cmp_lt_i32 s48, 1
	s_cbranch_scc1 .LBB0_984
	s_add_i32 s13, s48, 15
	s_add_i32 s12, s12, 0x21000
	s_lshr_b32 s49, s13, 4
	v_mov_b32_e32 v34, s12
	s_add_i32 s13, s49, 7
	ds_read_b32 v193, v34
	s_lshr_b32 s13, s13, 3
	s_lshl_b64 s[14:15], s[10:11], 20
	s_add_u32 s50, s14, 0x10000000
	s_addc_u32 s51, s15, 0
	s_lshl_b64 s[36:37], s[10:11], 16
	s_ashr_i32 s35, s34, 31
	s_cmp_lt_i32 s13, 2
	s_mov_b64 s[10:11], -1
	s_cbranch_scc1 .LBB0_1006
	s_cmp_lg_u32 s13, 2
	s_cbranch_scc0 .LBB0_986
	v_mov_b32_e32 v165, v0
	s_waitcnt lgkmcnt(0)
	v_add_u32_e32 v38, s34, v193
	v_readfirstlane_b32 s10, v165
	s_ashr_i32 s12, s10, 6
	v_and_b32_e32 v167, 15, v165
	s_mul_i32 s20, s12, 48
	v_or_b32_e32 v36, s20, v167
	v_cmp_gt_i32_e32 vcc, s48, v36
	v_and_b32_e32 v162, 48, v165
	v_lshl_add_u64 v[34:35], s[24:25], 0, v[162:163]
	v_cndmask_b32_e32 v36, 0, v36, vcc
	v_add_u32_e32 v36, v36, v38
	v_ashrrev_i32_e32 v37, 31, v36
	v_lshlrev_b64 v[36:37], 9, v[36:37]
	v_lshl_add_u64 v[36:37], v[34:35], 0, v[36:37]
	s_add_i32 s10, s20, 16
	global_load_dwordx4 v[66:69], v[36:37], off
	global_load_dwordx4 v[70:73], v[36:37], off offset:64
	global_load_dwordx4 v[74:77], v[36:37], off offset:128
	global_load_dwordx4 v[78:81], v[36:37], off offset:192
	global_load_dwordx4 v[82:85], v[36:37], off offset:256
	global_load_dwordx4 v[86:89], v[36:37], off offset:320
	global_load_dwordx4 v[90:93], v[36:37], off offset:384
	global_load_dwordx4 v[94:97], v[36:37], off offset:448
	v_or_b32_e32 v36, s10, v167
	v_cmp_gt_i32_e32 vcc, s48, v36
	s_add_i32 s10, s20, 32
	v_bfe_u32 v176, v165, 3, 3
	v_cndmask_b32_e32 v36, 0, v36, vcc
	v_add_u32_e32 v36, v36, v38
	v_ashrrev_i32_e32 v37, 31, v36
	v_lshlrev_b64 v[36:37], 9, v[36:37]
	v_lshl_add_u64 v[36:37], v[34:35], 0, v[36:37]
	global_load_dwordx4 v[98:101], v[36:37], off
	global_load_dwordx4 v[102:105], v[36:37], off offset:64
	global_load_dwordx4 v[106:109], v[36:37], off offset:128
	global_load_dwordx4 v[110:113], v[36:37], off offset:192
	global_load_dwordx4 v[114:117], v[36:37], off offset:256
	global_load_dwordx4 v[118:121], v[36:37], off offset:320
	global_load_dwordx4 v[122:125], v[36:37], off offset:384
	global_load_dwordx4 v[126:129], v[36:37], off offset:448
	v_or_b32_e32 v36, s10, v167
	v_cmp_gt_i32_e32 vcc, s48, v36
	v_or_b32_e32 v44, s20, v176
	s_add_u32 s13, s8, s36
	v_cndmask_b32_e32 v36, 0, v36, vcc
	v_add_u32_e32 v36, v36, v38
	v_ashrrev_i32_e32 v37, 31, v36
	v_lshlrev_b64 v[36:37], 9, v[36:37]
	v_lshl_add_u64 v[34:35], v[34:35], 0, v[36:37]
	v_or_b32_e32 v36, 8, v44
	s_addc_u32 s15, s9, s37
	s_lshl_b64 s[10:11], s[34:35], 2
	v_cmp_gt_i32_e32 vcc, s48, v36
	v_add_u32_e32 v38, 16, v44
	s_add_u32 s14, s13, s10
	v_cndmask_b32_e32 v36, 0, v36, vcc
	v_cmp_gt_i32_e32 vcc, s48, v38
	v_add_u32_e32 v40, 24, v44
	s_addc_u32 s15, s15, s11
	v_cmp_gt_i32_e64 s[10:11], s48, v44
	v_cndmask_b32_e32 v38, 0, v38, vcc
	v_cmp_gt_i32_e32 vcc, s48, v40
	v_add_u32_e32 v42, 32, v44
	global_load_dwordx4 v[130:133], v[34:35], off
	global_load_dwordx4 v[134:137], v[34:35], off offset:64
	global_load_dwordx4 v[138:141], v[34:35], off offset:128
	global_load_dwordx4 v[142:145], v[34:35], off offset:192
	global_load_dwordx4 v[146:149], v[34:35], off offset:256
	global_load_dwordx4 v[150:153], v[34:35], off offset:320
	global_load_dwordx4 v[154:157], v[34:35], off offset:384
	global_load_dwordx4 v[158:161], v[34:35], off offset:448
	v_cndmask_b32_e64 v34, 0, v44, s[10:11]
	v_cndmask_b32_e32 v40, 0, v40, vcc
	v_cmp_gt_i32_e32 vcc, s48, v42
	v_add_u32_e32 v44, 40, v44
	v_ashrrev_i32_e32 v35, 31, v34
	v_cndmask_b32_e32 v42, 0, v42, vcc
	v_cmp_gt_i32_e32 vcc, s48, v44
	v_lshl_add_u64 v[34:35], v[34:35], 2, s[14:15]
	v_ashrrev_i32_e32 v37, 31, v36
	v_cndmask_b32_e32 v44, 0, v44, vcc
	v_ashrrev_i32_e32 v39, 31, v38
	v_ashrrev_i32_e32 v41, 31, v40
	v_ashrrev_i32_e32 v43, 31, v42
	v_ashrrev_i32_e32 v45, 31, v44
	v_lshl_add_u64 v[36:37], v[36:37], 2, s[14:15]
	v_lshl_add_u64 v[38:39], v[38:39], 2, s[14:15]
	v_lshl_add_u64 v[40:41], v[40:41], 2, s[14:15]
	v_lshl_add_u64 v[42:43], v[42:43], 2, s[14:15]
	v_lshl_add_u64 v[44:45], v[44:45], 2, s[14:15]
	global_load_dword v174, v[34:35], off
	global_load_dword v172, v[36:37], off
	global_load_dword v170, v[38:39], off
	global_load_dword v168, v[40:41], off
	global_load_dword v166, v[42:43], off
	global_load_dword v164, v[44:45], off
	v_ashrrev_i32_e32 v34, 4, v165
	v_lshrrev_b32_e32 v36, 2, v34
	v_bfe_u32 v169, v165, 2, 2
	v_bfe_u32 v35, v34, 1, 1
	v_and_b32_e32 v36, 2, v36
	v_bitop3_b32 v35, v35, v169, v36 bitop3:0x36
	v_lshlrev_b32_e32 v36, 3, v165
	v_lshlrev_b32_e32 v35, 5, v35
	v_and_b32_e32 v162, 24, v36
	s_add_u32 s38, s4, s50
	v_lshlrev_b32_e32 v36, 4, v167
	v_lshl_add_u32 v37, v34, 7, 0
	s_addc_u32 s39, s5, s51
	v_add3_u32 v194, v37, v35, v162
	v_lshl_or_b32 v195, v34, 12, v36
	s_andn2_b64 vcc, exec, s[30:31]
	v_mov_b32_e32 v34, v2
	v_mov_b32_e32 v35, v3
	v_mov_b32_e32 v36, v4
	v_mov_b32_e32 v37, v5
	v_mov_b32_e32 v38, v6
	v_mov_b32_e32 v39, v7
	v_mov_b32_e32 v40, v8
	v_mov_b32_e32 v41, v9
	v_mov_b32_e32 v42, v10
	v_mov_b32_e32 v43, v11
	v_mov_b32_e32 v44, v12
	v_mov_b32_e32 v45, v13
	v_mov_b32_e32 v46, v14
	v_mov_b32_e32 v47, v15
	v_mov_b32_e32 v48, v16
	v_mov_b32_e32 v49, v17
	v_mov_b32_e32 v50, v18
	v_mov_b32_e32 v51, v19
	v_mov_b32_e32 v52, v20
	v_mov_b32_e32 v53, v21
	v_mov_b32_e32 v54, v22
	v_mov_b32_e32 v55, v23
	v_mov_b32_e32 v56, v24
	v_mov_b32_e32 v57, v25
	v_mov_b32_e32 v58, v26
	v_mov_b32_e32 v59, v27
	v_mov_b32_e32 v60, v28
	v_mov_b32_e32 v61, v29
	v_mov_b32_e32 v62, v30
	v_mov_b32_e32 v63, v31
	v_mov_b32_e32 v64, v32
	v_mov_b32_e32 v65, v33
	s_cbranch_vccnz .LBB0_965
	s_add_u32 s14, s38, 0x20000
	global_load_dwordx4 v[34:37], v195, s[38:39]
	s_addc_u32 s15, s39, 0
	global_load_dwordx4 v[38:41], v195, s[14:15]
	s_add_u32 s14, s38, 0x40000
	s_addc_u32 s15, s39, 0
	global_load_dwordx4 v[42:45], v195, s[14:15]
	s_add_u32 s14, s38, 0x60000
	s_addc_u32 s15, s39, 0
	global_load_dwordx4 v[46:49], v195, s[14:15]
	s_add_u32 s14, s38, 0x80000
	s_addc_u32 s15, s39, 0
	global_load_dwordx4 v[50:53], v195, s[14:15]
	s_add_u32 s14, s38, 0xa0000
	s_addc_u32 s15, s39, 0
	global_load_dwordx4 v[54:57], v195, s[14:15]
	s_add_u32 s14, s38, 0xc0000
	s_addc_u32 s15, s39, 0
	global_load_dwordx4 v[58:61], v195, s[14:15]
	s_add_u32 s14, s38, 0xe0000
	s_addc_u32 s15, s39, 0
	global_load_dwordx4 v[62:65], v195, s[14:15]
	s_add_u32 s14, s38, 0x100
	s_waitcnt vmcnt(0)
	s_addc_u32 s15, s39, 0
	v_cvt_pk_bf16_f32 v34, v34, v35
	v_cvt_pk_bf16_f32 v35, v36, v37
	v_cvt_pk_bf16_f32 v36, v38, v39
	v_cvt_pk_bf16_f32 v37, v40, v41
	ds_write2st64_b64 v194, v[34:35], v[36:37] offset1:8
	v_cvt_pk_bf16_f32 v34, v42, v43
	v_cvt_pk_bf16_f32 v35, v44, v45
	v_cvt_pk_bf16_f32 v36, v46, v47
	v_cvt_pk_bf16_f32 v37, v48, v49
	ds_write2st64_b64 v194, v[34:35], v[36:37] offset0:16 offset1:24
	v_cvt_pk_bf16_f32 v34, v50, v51
	v_cvt_pk_bf16_f32 v35, v52, v53
	v_cvt_pk_bf16_f32 v36, v54, v55
	v_cvt_pk_bf16_f32 v37, v56, v57
	ds_write2st64_b64 v194, v[34:35], v[36:37] offset0:32 offset1:40
	v_cvt_pk_bf16_f32 v34, v58, v59
	v_cvt_pk_bf16_f32 v35, v60, v61
	v_cvt_pk_bf16_f32 v36, v62, v63
	v_cvt_pk_bf16_f32 v37, v64, v65
	ds_write2st64_b64 v194, v[34:35], v[36:37] offset0:48 offset1:56
	global_load_dwordx4 v[34:37], v195, s[14:15]
	s_add_u32 s14, s38, 0x20100
	s_addc_u32 s15, s39, 0
	global_load_dwordx4 v[38:41], v195, s[14:15]
	s_add_u32 s14, s38, 0x40100
	s_addc_u32 s15, s39, 0
	global_load_dwordx4 v[42:45], v195, s[14:15]
	s_add_u32 s14, s38, 0x60100
	s_addc_u32 s15, s39, 0
	global_load_dwordx4 v[46:49], v195, s[14:15]
	s_add_u32 s14, s38, 0x80100
	s_addc_u32 s15, s39, 0
	global_load_dwordx4 v[50:53], v195, s[14:15]
	s_add_u32 s14, s38, 0xa0100
	s_addc_u32 s15, s39, 0
	global_load_dwordx4 v[54:57], v195, s[14:15]
	s_add_u32 s14, s38, 0xc0100
	s_addc_u32 s15, s39, 0
	global_load_dwordx4 v[58:61], v195, s[14:15]
	s_add_u32 s14, s38, 0xe0100
	s_addc_u32 s15, s39, 0
	global_load_dwordx4 v[62:65], v195, s[14:15]
